# ssm_pre dft_fold_rows: next row's 8 loads issued right after the current row is staged into LDS (second register set) instead of at the top of the next iteration
# baseline (speedup 1.0000x reference)
; __device__ void dft_fold_rows(KParams& p, int bid, int nb, char* smem) {
;     ...
;   for (int row = bid * 4 + w; row < NB * 1024; row += nb * 4) {
;     const bf16_t* A = p.ABt + (size_t)row * 4096;
;     bf16_t* F = p.Fs + (size_t)row * 2048;
;     __builtin_amdgcn_wave_barrier();
;     {
;       const uint4 q0 = *reinterpret_cast<const uint4*>(A + (0 * 64 + lane) * 8), q1 = *reinterpret_cast<const uint4*>(A + (1 * 64 + lane) * 8);
;       const uint4 q2 = *reinterpret_cast<const uint4*>(A + (2 * 64 + lane) * 8), q3 = *reinterpret_cast<const uint4*>(A + (3 * 64 + lane) * 8);
;       const uint4 q4 = *reinterpret_cast<const uint4*>(A + (4 * 64 + lane) * 8), q5 = *reinterpret_cast<const uint4*>(A + (5 * 64 + lane) * 8);
;       const uint4 q6 = *reinterpret_cast<const uint4*>(A + (6 * 64 + lane) * 8), q7 = *reinterpret_cast<const uint4*>(A + (7 * 64 + lane) * 8);
;       *reinterpret_cast<uint4*>(sr + (0 * 64 + lane) * 8) = q0; *reinterpret_cast<uint4*>(sr + (1 * 64 + lane) * 8) = q1;
;       *reinterpret_cast<uint4*>(sr + (2 * 64 + lane) * 8) = q2; *reinterpret_cast<uint4*>(sr + (3 * 64 + lane) * 8) = q3;
;       *reinterpret_cast<uint4*>(sr + (4 * 64 + lane) * 8) = q4; *reinterpret_cast<uint4*>(sr + (5 * 64 + lane) * 8) = q5;
;       *reinterpret_cast<uint4*>(sr + (6 * 64 + lane) * 8) = q6; *reinterpret_cast<uint4*>(sr + (7 * 64 + lane) * 8) = q7;
;     }
.Lgb_wd_4:
.LBB0_624:
	s_or_b64 exec, exec, s[6:7]
	s_movk_i32 s6, 0x1000
	s_mov_b64 s[14:15], s[0:1]
	v_cmp_gt_i32_e32 vcc, s6, v186
	s_waitcnt lgkmcnt(0)
	s_barrier
	s_and_saveexec_b64 s[10:11], vcc
	s_cbranch_execz .LBB0_633
	v_mbcnt_hi_u32_b32 v2, -1, v191
	v_and_b32_e32 v4, 64, v2
	v_xor_b32_e32 v3, 16, v2
	v_add_u32_e32 v4, 64, v4
	v_cmp_lt_i32_e32 vcc, v3, v4
	s_load_dwordx2 s[20:21], s[14:15], 0x178
	s_load_dwordx2 s[18:19], s[14:15], 0x1a0
	s_load_dwordx2 s[12:13], s[14:15], 0x228
	v_cndmask_b32_e32 v3, v2, v3, vcc
	v_lshlrev_b32_e32 v42, 2, v3
	v_xor_b32_e32 v3, 32, v2
	v_cmp_lt_i32_e32 vcc, v3, v4
	v_lshlrev_b32_e32 v40, 13, v143
	s_lshl_b32 s16, s34, 2
	v_cndmask_b32_e32 v2, v2, v3, vcc
	v_lshlrev_b32_e32 v43, 2, v2
	v_lshlrev_b32_e32 v2, 5, v184
	v_sub_u32_e32 v44, v40, v2
	v_lshlrev_b64 v[2:3], 13, v[186:187]
	v_or_b32_e32 v2, v2, v188
	s_waitcnt lgkmcnt(0)
	v_lshl_add_u64 v[2:3], s[18:19], 0, v[2:3]
	s_mov_b64 s[18:19], 0x1c00
	v_lshl_add_u64 v[34:35], v[2:3], 0, s[18:19]
	v_lshlrev_b64 v[2:3], 12, v[186:187]
	v_or_b32_e32 v41, v40, v188
	s_ashr_i32 s17, s16, 31
	v_lshl_or_b32 v2, v184, 5, v2
	v_cmp_eq_u32_e64 s[6:7], 0, v184
	v_cmp_ne_u32_e64 s[8:9], 0, v184
	s_lshl_b64 s[18:19], s[16:17], 13
	v_lshl_add_u64 v[36:37], s[20:21], 0, v[2:3]
	s_lshl_b64 s[20:21], s[16:17], 12
	s_mov_b64 s[22:23], 0
	v_add_u32_e32 v45, v41, v188
	v_mov_b32_e32 v39, 0
	s_movk_i32 s17, 0xfff
	v_mov_b32_e32 v46, v186
	v_add_co_u32_e32 v196, vcc, 0xfffff000, v34
	s_nop 1
	v_addc_co_u32_e32 v197, vcc, -1, v35, vcc
	global_load_dwordx4 v[144:147], v[34:35], off offset:-3072
	global_load_dwordx4 v[148:151], v[34:35], off offset:-2048
	global_load_dwordx4 v[152:155], v[34:35], off offset:-1024
	global_load_dwordx4 v[156:159], v[34:35], off
	global_load_dwordx4 v[160:163], v[196:197], off offset:-3072
	global_load_dwordx4 v[164:167], v[196:197], off offset:-2048
	global_load_dwordx4 v[168:171], v[196:197], off offset:-1024
	global_load_dwordx4 v[172:175], v[34:35], off offset:-4096
	s_branch .LBB0_627

; __device__ __forceinline__ float bf2f(bf16_t h) { return __uint_as_float(((uint32_t)h) << 16); }
; __device__ void dft_fold_rows(KParams& p, int bid, int nb, char* smem) {
;     ...
;     __builtin_amdgcn_wave_barrier();
;     {
;       const uint4 q0 = *reinterpret_cast<const uint4*>(A + (0 * 64 + lane) * 8), q1 = *reinterpret_cast<const uint4*>(A + (1 * 64 + lane) * 8);
;       const uint4 q2 = *reinterpret_cast<const uint4*>(A + (2 * 64 + lane) * 8), q3 = *reinterpret_cast<const uint4*>(A + (3 * 64 + lane) * 8);
;       const uint4 q4 = *reinterpret_cast<const uint4*>(A + (4 * 64 + lane) * 8), q5 = *reinterpret_cast<const uint4*>(A + (5 * 64 + lane) * 8);
;       const uint4 q6 = *reinterpret_cast<const uint4*>(A + (6 * 64 + lane) * 8), q7 = *reinterpret_cast<const uint4*>(A + (7 * 64 + lane) * 8);
;       *reinterpret_cast<uint4*>(sr + (0 * 64 + lane) * 8) = q0; *reinterpret_cast<uint4*>(sr + (1 * 64 + lane) * 8) = q1;
;       *reinterpret_cast<uint4*>(sr + (2 * 64 + lane) * 8) = q2; *reinterpret_cast<uint4*>(sr + (3 * 64 + lane) * 8) = q3;
;       *reinterpret_cast<uint4*>(sr + (4 * 64 + lane) * 8) = q4; *reinterpret_cast<uint4*>(sr + (5 * 64 + lane) * 8) = q5;
;       *reinterpret_cast<uint4*>(sr + (6 * 64 + lane) * 8) = q6; *reinterpret_cast<uint4*>(sr + (7 * 64 + lane) * 8) = q7;
;     }
;     __builtin_amdgcn_wave_barrier();
;     const int l0 = lane * 16;
;     float alt = 0.f;
;     uint32_t oa[8], ob[8];
; #pragma unroll
;     for (int half = 0; half < 2; ++half) {
;       const bf16_t* base = sr + half * 2048;
;       const uint4 fa = *reinterpret_cast<const uint4*>(base + l0), fb = *reinterpret_cast<const uint4*>(base + l0 + 8);
;       const uint4 ra = *reinterpret_cast<const uint4*>(base + 2032 - l0), rb = *reinterpret_cast<const uint4*>(base + 2040 - l0);
;       const float r16 = (lane > 0) ? bf2f(base[2048 - l0]) : 0.f;
.LBB0_627:
	v_add_co_u32_e32 v48, vcc, 0xfffff000, v34
	v_mov_b32_e32 v47, 0
	s_nop 0
	v_addc_co_u32_e32 v49, vcc, -1, v35, vcc
	s_waitcnt lgkmcnt(0)
	s_waitcnt vmcnt(0)
	ds_write_b128 v41, v[144:147] offset:4096
	ds_write_b128 v41, v[148:151] offset:5120
	ds_write_b128 v41, v[152:155] offset:6144
	ds_write_b128 v41, v[156:159] offset:7168
	ds_write_b128 v41, v[160:163]
	ds_write_b128 v41, v[164:167] offset:1024
	ds_write_b128 v41, v[168:171] offset:2048
	ds_write_b128 v41, v[172:175] offset:3072
	v_lshl_add_u64 v[176:177], v[34:35], 0, s[18:19]
	v_add_co_u32_e32 v196, vcc, 0xfffff000, v176
	s_nop 1
	v_addc_co_u32_e32 v197, vcc, -1, v177, vcc
	global_load_dwordx4 v[144:147], v[176:177], off offset:-3072
	global_load_dwordx4 v[148:151], v[176:177], off offset:-2048
	global_load_dwordx4 v[152:155], v[176:177], off offset:-1024
	global_load_dwordx4 v[156:159], v[176:177], off
	global_load_dwordx4 v[160:163], v[196:197], off offset:-3072
	global_load_dwordx4 v[164:167], v[196:197], off offset:-2048
	global_load_dwordx4 v[168:171], v[196:197], off offset:-1024
	global_load_dwordx4 v[172:175], v[176:177], off offset:-4096
	ds_read_b128 v[30:33], v45
	ds_read_b128 v[18:21], v45 offset:16
	ds_read_b128 v[22:25], v44 offset:4064
	ds_read_b128 v[26:29], v44 offset:4080
	s_and_saveexec_b64 s[24:25], s[8:9]
	s_cbranch_execz .LBB0_629
	ds_read_u16 v2, v44 offset:4096
	s_waitcnt lgkmcnt(0)
	v_lshlrev_b32_e32 v47, 16, v2
